# unused
# baseline (speedup 1.0000x reference)
; #define PG8_STAGE(bufoff, gbase, v0, v1) do { \
;         __builtin_amdgcn_global_load_lds((const unsigned*)((const char*)(gbase) + (v0)), (LAS unsigned*)(lds + (bufoff) + ldsw), 16, 0, 0); \
;         __builtin_amdgcn_global_load_lds((const unsigned*)((const char*)(gbase) + (v1)), (LAS unsigned*)(lds + (bufoff) + ldsw + 8192), 16, 0, 0); } while (0)
; #define PG8_LDA(dst, b, h) do { _Pragma("unroll") for (int m = 0; m < 4; ++m) _Pragma("unroll") for (int k = 0; k < 2; ++k) dst[m][k] = *(const LAS bf16x8*)(lds + PG8_SA(b, h) + aoff + m * 2048 + k * 1024); } while (0)
; #define PG8_LDB(dst, b, h) do { _Pragma("unroll") for (int n = 0; n < 2; ++n) _Pragma("unroll") for (int k = 0; k < 2; ++k) dst[n][k] = *(const LAS bf16x8*)(lds + PG8_SB(b, h) + boff + n * 2048 + k * 1024); } while (0)
; #define PG8_MMA(ai, bj, At, Bt) do { __builtin_amdgcn_s_setprio(1); _Pragma("unroll") for (int m = 0; m < 4; ++m) _Pragma("unroll") for (int n = 0; n < 2; ++n) _Pragma("unroll") for (int k = 0; k < 2; ++k) \
;         acc[ai][bj][m][n] = __builtin_amdgcn_mfma_f32_16x16x32_bf16(Bt[n][k], At[m][k], acc[ai][bj][m][n], 0, 0, 0); __builtin_amdgcn_s_setprio(0); } while (0)
; #define PG8_WAIT_V(n) asm volatile("s_waitcnt vmcnt(" #n ")" ::: "memory")
; #define PG8_BAR __builtin_amdgcn_s_barrier()
; #define PG8_SCHED __builtin_amdgcn_sched_barrier(0)
; template <class Epi, class Sched>
; __device__ __forceinline__ void gemm_phase(LAS unsigned char* lds, const int K, const Sched& S, const Epi& E) {
;     ...
;             PG8_WAIT_V(6); PG8_BAR; PG8_MMA(1, 1, At, B1); PG8_BAR;
;             PG8_LDB(B0, 1, 0); PG8_SCHED; PG8_LDA(At, 1, 0); PG8_STAGE(PG8_SA(0, 1), a2, x10, x11);
; __device__ __forceinline__ bool bg_decode(int st, int wg, int NW, int lane, KP kp, const float*& src, int& ldS, bf16_t*& dst, int& o2) {
;     ...
;     const int l = g / 98304, r = g - l * 98304;
;     unsigned char* ws = kp->ws;
;     if (r < 65536) {
;         const int e = r >> 10, kc = (r >> 2) & 255, kind = (r >> 1) & 1, cc = r & 1, n = cc * 256 + lane;
;         ldS = FF; o2 = 256 * 8;
;         src = kp->in[27 + kind] + ((size_t)(l * NE + e) * D + kc * 8) * FF + n;
;         const int drow = (n >> 7) * 256 + kind * 128 + (n & 127);
;         dst = (bf16_t*)(ws + WS_WGU) + l * WGU_L + (size_t)e * 1024 * D + ((size_t)kc * 1024 + drow) * 8;
.Lpb8_p4j:
	s_barrier
	s_setprio 1
	v_mfma_f32_16x16x32_bf16 v[54:57], v[212:215], v[176:179], v[54:57]
	v_mfma_f32_16x16x32_bf16 v[50:53], v[220:223], v[176:179], v[50:53]
	v_mfma_f32_16x16x32_bf16 v[38:41], v[212:215], v[184:187], v[38:41]
	v_mfma_f32_16x16x32_bf16 v[34:37], v[220:223], v[184:187], v[34:37]
	v_mfma_f32_16x16x32_bf16 v[22:25], v[212:215], v[192:195], v[22:25]
	v_mfma_f32_16x16x32_bf16 v[18:21], v[220:223], v[192:195], v[18:21]
	v_mfma_f32_16x16x32_bf16 v[6:9], v[212:215], v[200:203], v[6:9]
	v_mfma_f32_16x16x32_bf16 v[2:5], v[220:223], v[200:203], v[2:5]
	v_mfma_f32_16x16x32_bf16 v[54:57], v[216:219], v[180:183], v[54:57]
	v_mfma_f32_16x16x32_bf16 v[50:53], v[224:227], v[180:183], v[50:53]
	v_mfma_f32_16x16x32_bf16 v[38:41], v[216:219], v[188:191], v[38:41]
	v_mfma_f32_16x16x32_bf16 v[34:37], v[224:227], v[188:191], v[34:37]
	v_mfma_f32_16x16x32_bf16 v[22:25], v[216:219], v[196:199], v[22:25]
	v_mfma_f32_16x16x32_bf16 v[18:21], v[224:227], v[196:199], v[18:21]
	v_mfma_f32_16x16x32_bf16 v[6:9], v[216:219], v[208:211], v[6:9]
	v_mfma_f32_16x16x32_bf16 v[2:5], v[224:227], v[208:211], v[2:5]
	s_setprio 0
	s_add_i32 s55, 0, 0x18000
	v_add_u32_e32 v134, s55, v149
	s_barrier
	ds_read_b128 v[160:163], v134
	ds_read_b128 v[164:167], v134 offset:1024
	ds_read_b128 v[168:171], v134 offset:2048
	ds_read_b128 v[172:175], v134 offset:3072
	s_mov_b32 m0, s39
	ds_read_b128 v[176:179], v151 offset:32768
	ds_read_b128 v[180:183], v151 offset:33792
	ds_read_b128 v[184:187], v151 offset:34816
	ds_read_b128 v[188:191], v151 offset:35840
	ds_read_b128 v[192:195], v151 offset:36864
	ds_read_b128 v[196:199], v151 offset:37888
	ds_read_b128 v[200:203], v151 offset:38912
	ds_read_b128 v[208:211], v151 offset:39936
	v_cndmask_b32_e32 v134, v140, v153, vcc
	global_load_lds_dwordx4 v139, s[26:27]
	s_mov_b32 m0, s40
	s_nop 0
	global_load_lds_dwordx4 v134, s[26:27]
	s_add_u32 s90, s90, 1
	s_cmp_lt_u32 s90, 4
	s_cbranch_scc1 .Lpb8_p5n
	s_mov_b32 s90, 0
	s_cmp_ge_u32 s70, 0x28000
	s_cbranch_scc1 .Lpb8_p5n
	s_cmp_eq_u32 s80, 0
	s_cbranch_scc0 .Lpb8_adv4
	s_cmp_ge_u32 s70, 0x18000
	s_cselect_b32 s84, 0x18000, 0
	s_cselect_b32 s83, 0x10000000, 0
	s_mov_b32 s81, 0x4030000
	s_cselect_b32 s81, 0x14430000, s81
	s_sub_u32 s84, s70, s84
	s_lshr_b32 s85, s84, 2
	s_lshl_b32 s85, s85, 14
	s_and_b32 s86, s84, 1
	s_lshl_b32 s87, s86, 10
	s_add_u32 s87, s87, s85
	s_add_u32 s87, s87, s83
	s_bitcmp1_b32 s84, 1
	s_cselect_b64 s[72:73], s[76:77], s[74:75]
	s_add_u32 s72, s72, s87
	s_addc_u32 s73, s73, 0
	s_add_u32 s88, s72, 0x2000
	s_addc_u32 s89, s73, 0
	s_lshl_b32 s86, s86, 13
	s_add_u32 s85, s85, s86
	s_and_b32 s86, s84, 2
	s_lshl_b32 s86, s86, 10
	s_add_u32 s85, s85, s86
	s_add_u32 s85, s85, s81
	v_add_u32_e32 v253, s85, v252
	s_movk_i32 s81, 0x400
	s_branch .Lpb8_ld4

; #define PG8_STAGE(bufoff, gbase, v0, v1) do { \
;         __builtin_amdgcn_global_load_lds((const unsigned*)((const char*)(gbase) + (v0)), (LAS unsigned*)(lds + (bufoff) + ldsw), 16, 0, 0); \
;         __builtin_amdgcn_global_load_lds((const unsigned*)((const char*)(gbase) + (v1)), (LAS unsigned*)(lds + (bufoff) + ldsw + 8192), 16, 0, 0); } while (0)
; #define PG8_LDA(dst, b, h) do { _Pragma("unroll") for (int m = 0; m < 4; ++m) _Pragma("unroll") for (int k = 0; k < 2; ++k) dst[m][k] = *(const LAS bf16x8*)(lds + PG8_SA(b, h) + aoff + m * 2048 + k * 1024); } while (0)
; #define PG8_LDB(dst, b, h) do { _Pragma("unroll") for (int n = 0; n < 2; ++n) _Pragma("unroll") for (int k = 0; k < 2; ++k) dst[n][k] = *(const LAS bf16x8*)(lds + PG8_SB(b, h) + boff + n * 2048 + k * 1024); } while (0)
; #define PG8_MMA(ai, bj, At, Bt) do { __builtin_amdgcn_s_setprio(1); _Pragma("unroll") for (int m = 0; m < 4; ++m) _Pragma("unroll") for (int n = 0; n < 2; ++n) _Pragma("unroll") for (int k = 0; k < 2; ++k) \
;         acc[ai][bj][m][n] = __builtin_amdgcn_mfma_f32_16x16x32_bf16(Bt[n][k], At[m][k], acc[ai][bj][m][n], 0, 0, 0); __builtin_amdgcn_s_setprio(0); } while (0)
; #define PG8_WAIT_V(n) asm volatile("s_waitcnt vmcnt(" #n ")" ::: "memory")
; #define PG8_BAR __builtin_amdgcn_s_barrier()
; #define PG8_SCHED __builtin_amdgcn_sched_barrier(0)
; template <class Epi, class Sched>
; __device__ __forceinline__ void gemm_phase(LAS unsigned char* lds, const int K, const Sched& S, const Epi& E) {
;     ...
;             PG8_WAIT_V(6); PG8_BAR; PG8_MMA(1, 1, At, B1); PG8_BAR;
;             PG8_LDB(B0, 1, 0); PG8_SCHED; PG8_LDA(At, 1, 0); PG8_STAGE(PG8_SA(0, 1), a2, x10, x11);
; __device__ __forceinline__ bool bg_decode(int st, int wg, int NW, int lane, KP kp, const float*& src, int& ldS, bf16_t*& dst, int& o2) {
;     ...
;     const int l = g / 98304, r = g - l * 98304;
;     unsigned char* ws = kp->ws;
;     if (r < 65536) {
;         const int e = r >> 10, kc = (r >> 2) & 255, kind = (r >> 1) & 1, cc = r & 1, n = cc * 256 + lane;
;         ldS = FF; o2 = 256 * 8;
;         src = kp->in[27 + kind] + ((size_t)(l * NE + e) * D + kc * 8) * FF + n;
;         const int drow = (n >> 7) * 256 + kind * 128 + (n & 127);
;         dst = (bf16_t*)(ws + WS_WGU) + l * WGU_L + (size_t)e * 1024 * D + ((size_t)kc * 1024 + drow) * 8;
.Lpb9_p4j:
	s_barrier
	s_setprio 1
	v_mfma_f32_16x16x32_bf16 v[54:57], v[216:219], v[180:183], v[54:57]
	v_mfma_f32_16x16x32_bf16 v[50:53], v[224:227], v[180:183], v[50:53]
	v_mfma_f32_16x16x32_bf16 v[38:41], v[216:219], v[188:191], v[38:41]
	v_mfma_f32_16x16x32_bf16 v[34:37], v[224:227], v[188:191], v[34:37]
	v_mfma_f32_16x16x32_bf16 v[22:25], v[216:219], v[196:199], v[22:25]
	v_mfma_f32_16x16x32_bf16 v[18:21], v[224:227], v[196:199], v[18:21]
	v_mfma_f32_16x16x32_bf16 v[6:9], v[216:219], v[208:211], v[6:9]
	v_mfma_f32_16x16x32_bf16 v[2:5], v[224:227], v[208:211], v[2:5]
	v_mfma_f32_16x16x32_bf16 v[54:57], v[220:223], v[184:187], v[54:57]
	v_mfma_f32_16x16x32_bf16 v[50:53], v[228:231], v[184:187], v[50:53]
	v_mfma_f32_16x16x32_bf16 v[38:41], v[220:223], v[192:195], v[38:41]
	v_mfma_f32_16x16x32_bf16 v[34:37], v[228:231], v[192:195], v[34:37]
	v_mfma_f32_16x16x32_bf16 v[22:25], v[220:223], v[200:203], v[22:25]
	v_mfma_f32_16x16x32_bf16 v[18:21], v[228:231], v[200:203], v[18:21]
	v_mfma_f32_16x16x32_bf16 v[6:9], v[220:223], v[212:215], v[6:9]
	v_mfma_f32_16x16x32_bf16 v[2:5], v[228:231], v[212:215], v[2:5]
	s_setprio 0
	s_add_i32 s67, 0, 0x18000
	v_add_u32_e32 v134, s67, v151
	s_barrier
	ds_read_b128 v[164:167], v134
	ds_read_b128 v[168:171], v134 offset:1024
	ds_read_b128 v[172:175], v134 offset:2048
	ds_read_b128 v[176:179], v134 offset:3072
	s_mov_b32 m0, s51
	ds_read_b128 v[180:183], v154 offset:32768
	ds_read_b128 v[184:187], v154 offset:33792
	ds_read_b128 v[188:191], v154 offset:34816
	ds_read_b128 v[192:195], v154 offset:35840
	ds_read_b128 v[196:199], v154 offset:36864
	ds_read_b128 v[200:203], v154 offset:37888
	ds_read_b128 v[208:211], v154 offset:38912
	ds_read_b128 v[212:215], v154 offset:39936
	v_cndmask_b32_e32 v134, v140, v160, vcc
	global_load_lds_dwordx4 v139, s[44:45]
	s_mov_b32 m0, s52
	s_nop 0
	global_load_lds_dwordx4 v134, s[44:45]
	s_add_u32 s90, s90, 1
	s_cmp_lt_u32 s90, 2
	s_cbranch_scc1 .Lpb9_p5n
	s_mov_b32 s90, 0
	s_cmp_ge_u32 s70, 0x24000
	s_cbranch_scc1 .Lpb9_p5n
	s_cmp_eq_u32 s80, 0
	s_cbranch_scc0 .Lpb9_adv2
	s_cmp_ge_u32 s70, 0x18000
	s_cselect_b32 s84, 0x18000, 0
	s_cselect_b32 s83, 0x10000000, 0
	s_mov_b32 s81, 0x4030000
	s_cselect_b32 s81, 0x14430000, s81
	s_sub_u32 s84, s70, s84
	s_lshr_b32 s85, s84, 2
	s_lshl_b32 s85, s85, 14
	s_and_b32 s86, s84, 1
	s_lshl_b32 s87, s86, 10
	s_add_u32 s87, s87, s85
	s_add_u32 s87, s87, s83
	s_bitcmp1_b32 s84, 1
	s_cselect_b64 s[72:73], s[76:77], s[74:75]
	s_add_u32 s72, s72, s87
	s_addc_u32 s73, s73, 0
	s_add_u32 s88, s72, 0x2000
	s_addc_u32 s89, s73, 0
	s_lshl_b32 s86, s86, 13
	s_add_u32 s85, s85, s86
	s_and_b32 s86, s84, 2
	s_lshl_b32 s86, s86, 10
	s_add_u32 s85, s85, s86
	s_add_u32 s85, s85, s81
	v_add_u32_e32 v253, s85, v252
	s_movk_i32 s81, 0x400
	s_branch .Lpb9_ld2

; #define PG8_STAGE(bufoff, gbase, v0, v1) do { \
;         __builtin_amdgcn_global_load_lds((const unsigned*)((const char*)(gbase) + (v0)), (LAS unsigned*)(lds + (bufoff) + ldsw), 16, 0, 0); \
;         __builtin_amdgcn_global_load_lds((const unsigned*)((const char*)(gbase) + (v1)), (LAS unsigned*)(lds + (bufoff) + ldsw + 8192), 16, 0, 0); } while (0)
; #define PG8_LDA(dst, b, h) do { _Pragma("unroll") for (int m = 0; m < 4; ++m) _Pragma("unroll") for (int k = 0; k < 2; ++k) dst[m][k] = *(const LAS bf16x8*)(lds + PG8_SA(b, h) + aoff + m * 2048 + k * 1024); } while (0)
; #define PG8_LDB(dst, b, h) do { _Pragma("unroll") for (int n = 0; n < 2; ++n) _Pragma("unroll") for (int k = 0; k < 2; ++k) dst[n][k] = *(const LAS bf16x8*)(lds + PG8_SB(b, h) + boff + n * 2048 + k * 1024); } while (0)
; #define PG8_MMA(ai, bj, At, Bt) do { __builtin_amdgcn_s_setprio(1); _Pragma("unroll") for (int m = 0; m < 4; ++m) _Pragma("unroll") for (int n = 0; n < 2; ++n) _Pragma("unroll") for (int k = 0; k < 2; ++k) \
;         acc[ai][bj][m][n] = __builtin_amdgcn_mfma_f32_16x16x32_bf16(Bt[n][k], At[m][k], acc[ai][bj][m][n], 0, 0, 0); __builtin_amdgcn_s_setprio(0); } while (0)
; #define PG8_WAIT_V(n) asm volatile("s_waitcnt vmcnt(" #n ")" ::: "memory")
; #define PG8_BAR __builtin_amdgcn_s_barrier()
; #define PG8_SCHED __builtin_amdgcn_sched_barrier(0)
; template <class Epi, class Sched>
; __device__ __forceinline__ void gemm_phase(LAS unsigned char* lds, const int K, const Sched& S, const Epi& E) {
;     ...
;             PG8_WAIT_V(6); PG8_BAR; PG8_MMA(1, 1, At, B1); PG8_BAR;
;             PG8_LDB(B0, 1, 0); PG8_SCHED; PG8_LDA(At, 1, 0); PG8_STAGE(PG8_SA(0, 1), a2, x10, x11);
; __device__ __forceinline__ bool bg_decode(int st, int wg, int NW, int lane, KP kp, const float*& src, int& ldS, bf16_t*& dst, int& o2) {
;     ...
;     } else {
;         const int r2 = r - 65536, e = r2 >> 9, kc = (r2 >> 3) & 63, cc = r2 & 7, n = cc * 256 + lane;
;         ldS = D; o2 = 128 * 8;
;         src = kp->in[29] + ((size_t)(l * NE + e) * FF + kc * 8) * D + n;
;         dst = (bf16_t*)(ws + WS_WD) + l * WD_L + (size_t)e * D * FF + ((size_t)kc * D + n) * 8;
.Lpb17_p4j:
	s_barrier
	s_setprio 1
	v_mfma_f32_16x16x32_bf16 v[54:57], v[208:211], v[176:179], v[54:57]
	v_mfma_f32_16x16x32_bf16 v[50:53], v[216:219], v[176:179], v[50:53]
	v_mfma_f32_16x16x32_bf16 v[38:41], v[208:211], v[184:187], v[38:41]
	v_mfma_f32_16x16x32_bf16 v[34:37], v[216:219], v[184:187], v[34:37]
	v_mfma_f32_16x16x32_bf16 v[22:25], v[208:211], v[192:195], v[22:25]
	v_mfma_f32_16x16x32_bf16 v[18:21], v[216:219], v[192:195], v[18:21]
	v_mfma_f32_16x16x32_bf16 v[6:9], v[208:211], v[200:203], v[6:9]
	v_mfma_f32_16x16x32_bf16 v[2:5], v[216:219], v[200:203], v[2:5]
	v_mfma_f32_16x16x32_bf16 v[54:57], v[212:215], v[180:183], v[54:57]
	v_mfma_f32_16x16x32_bf16 v[50:53], v[220:223], v[180:183], v[50:53]
	v_mfma_f32_16x16x32_bf16 v[38:41], v[212:215], v[188:191], v[38:41]
	v_mfma_f32_16x16x32_bf16 v[34:37], v[220:223], v[188:191], v[34:37]
	v_mfma_f32_16x16x32_bf16 v[22:25], v[212:215], v[196:199], v[22:25]
	v_mfma_f32_16x16x32_bf16 v[18:21], v[220:223], v[196:199], v[18:21]
	v_mfma_f32_16x16x32_bf16 v[6:9], v[212:215], v[204:207], v[6:9]
	v_mfma_f32_16x16x32_bf16 v[2:5], v[220:223], v[204:207], v[2:5]
	s_setprio 0
	s_add_i32 s54, 0, 0x18000
	v_add_u32_e32 v134, s54, v149
	s_barrier
	ds_read_b128 v[160:163], v134
	ds_read_b128 v[164:167], v134 offset:1024
	ds_read_b128 v[168:171], v134 offset:2048
	ds_read_b128 v[172:175], v134 offset:3072
	s_mov_b32 m0, s39
	ds_read_b128 v[176:179], v151 offset:32768
	ds_read_b128 v[180:183], v151 offset:33792
	ds_read_b128 v[184:187], v151 offset:34816
	ds_read_b128 v[188:191], v151 offset:35840
	ds_read_b128 v[192:195], v151 offset:36864
	ds_read_b128 v[196:199], v151 offset:37888
	ds_read_b128 v[200:203], v151 offset:38912
	ds_read_b128 v[204:207], v151 offset:39936
	v_cndmask_b32_e32 v134, v140, v153, vcc
	global_load_lds_dwordx4 v139, s[26:27]
	s_mov_b32 m0, s40
	s_nop 0
	global_load_lds_dwordx4 v134, s[26:27]
	s_add_u32 s90, s90, 1
	s_cmp_lt_u32 s90, 3
	s_cbranch_scc1 .Lpb17_p5n
	s_mov_b32 s90, 0
	s_cmp_ge_u32 s70, 0x30000
	s_cbranch_scc1 .Lpb17_p5n
	s_cmp_eq_u32 s80, 0
	s_cbranch_scc0 .Lpb17_adv6
	s_cmp_ge_u32 s70, 0x28000
	s_mov_b32 s84, 0x10000
	s_cselect_b32 s84, 0x28000, s84
	s_cselect_b32 s83, 0x10000000, 0
	s_mov_b32 s81, 0x24830000
	s_cselect_b32 s81, 0x2ca30000, s81
	s_sub_u32 s84, s70, s84
	s_lshr_b32 s85, s84, 3
	s_and_b32 s86, s84, 7
	s_lshl_b32 s87, s85, 16
	s_lshl_b32 s84, s86, 10
	s_add_u32 s87, s87, s84
	s_add_u32 s87, s87, s83
	s_add_u32 s72, s74, s87
	s_addc_u32 s73, s75, 0
	s_add_u32 s88, s72, 0x8000
	s_addc_u32 s89, s73, 0
	s_lshl_b32 s85, s85, 15
	s_lshl_b32 s86, s86, 12
	s_add_u32 s85, s85, s86
	s_add_u32 s85, s85, s81
	v_add_u32_e32 v253, s85, v252
	s_branch .Lpb17_ld6
